# the five main loop labels (GEMM K-loops, attention) 64-byte aligned with the padding outside the loops
# speedup vs baseline: 1.0016x; 1.0016x over previous
.Lrope_skip_ft:
	s_waitcnt vmcnt(8)
	s_waitcnt lgkmcnt(0)
	s_barrier
	s_setprio 1
	s_waitcnt lgkmcnt(7)
	v_mfma_f32_16x16x32_bf16 v[62:65], v[130:133], v[162:165], 0
	v_mfma_f32_16x16x32_bf16 v[58:61], v[134:137], v[162:165], 0
	s_waitcnt lgkmcnt(6)
	v_mfma_f32_16x16x32_bf16 v[54:57], v[130:133], v[166:169], 0
	v_mfma_f32_16x16x32_bf16 v[50:53], v[134:137], v[166:169], 0
	s_waitcnt lgkmcnt(3)
	v_mfma_f32_16x16x32_bf16 v[46:49], v[130:133], v[178:181], 0
	v_mfma_f32_16x16x32_bf16 v[42:45], v[134:137], v[178:181], 0
	s_waitcnt lgkmcnt(2)
	v_mfma_f32_16x16x32_bf16 v[38:41], v[130:133], v[182:185], 0
	v_mfma_f32_16x16x32_bf16 v[34:37], v[134:137], v[182:185], 0
	v_mfma_f32_16x16x32_bf16 v[62:65], v[138:141], v[170:173], v[62:65]
	v_mfma_f32_16x16x32_bf16 v[58:61], v[142:145], v[170:173], v[58:61]
	v_mfma_f32_16x16x32_bf16 v[54:57], v[138:141], v[174:177], v[54:57]
	v_mfma_f32_16x16x32_bf16 v[50:53], v[142:145], v[174:177], v[50:53]
	s_waitcnt lgkmcnt(1)
	v_mfma_f32_16x16x32_bf16 v[46:49], v[138:141], v[186:189], v[46:49]
	v_mfma_f32_16x16x32_bf16 v[42:45], v[142:145], v[186:189], v[42:45]
	s_waitcnt lgkmcnt(0)
	v_mfma_f32_16x16x32_bf16 v[38:41], v[138:141], v[190:193], v[38:41]
	v_mfma_f32_16x16x32_bf16 v[34:37], v[142:145], v[190:193], v[34:37]
	s_setprio 0
	s_setprio 1
	v_mfma_f32_16x16x32_bf16 v[30:33], v[146:149], v[162:165], 0
	v_mfma_f32_16x16x32_bf16 v[26:29], v[150:153], v[162:165], 0
	v_mfma_f32_16x16x32_bf16 v[22:25], v[146:149], v[166:169], 0
	v_mfma_f32_16x16x32_bf16 v[18:21], v[150:153], v[166:169], 0
	v_mfma_f32_16x16x32_bf16 v[14:17], v[146:149], v[178:181], 0
	v_mfma_f32_16x16x32_bf16 v[10:13], v[150:153], v[178:181], 0
	v_mfma_f32_16x16x32_bf16 v[6:9], v[146:149], v[182:185], 0
	v_mfma_f32_16x16x32_bf16 v[2:5], v[150:153], v[182:185], 0
	v_mfma_f32_16x16x32_bf16 v[30:33], v[154:157], v[170:173], v[30:33]
	v_mfma_f32_16x16x32_bf16 v[26:29], v[158:161], v[170:173], v[26:29]
	v_mfma_f32_16x16x32_bf16 v[22:25], v[154:157], v[174:177], v[22:25]
	v_mfma_f32_16x16x32_bf16 v[18:21], v[158:161], v[174:177], v[18:21]
	v_mfma_f32_16x16x32_bf16 v[14:17], v[154:157], v[186:189], v[14:17]
	v_mfma_f32_16x16x32_bf16 v[10:13], v[158:161], v[186:189], v[10:13]
	v_mfma_f32_16x16x32_bf16 v[6:9], v[154:157], v[190:193], v[6:9]
	v_mfma_f32_16x16x32_bf16 v[2:5], v[158:161], v[190:193], v[2:5]
	s_setprio 0
	s_barrier
	s_add_i32 s78, 0, 0x18000
	v_add_u32_e32 v162, s78, v217
	v_add_u32_e32 v163, s78, v218
	s_add_i32 s78, 0, 0x1c000
	v_add_u32_e32 v164, s78, v217
	ds_read_b128 v[130:133], v162
	ds_read_b128 v[134:137], v162 offset:2048
	ds_read_b128 v[138:141], v163
	ds_read_b128 v[142:145], v163 offset:2048
	v_add_u32_e32 v165, s78, v218
	ds_read_b128 v[146:149], v164
	ds_read_b128 v[150:153], v164 offset:2048
	ds_read_b128 v[154:157], v165
	ds_read_b128 v[158:161], v165 offset:2048
	ds_read_b128 v[166:169], v223 offset:32768
	ds_read_b128 v[170:173], v223 offset:34816
	ds_read_b128 v[174:177], v224 offset:32768
	ds_read_b128 v[178:181], v224 offset:34816
	ds_read_b128 v[182:185], v223 offset:36864
	ds_read_b128 v[186:189], v223 offset:38912
	ds_read_b128 v[190:193], v224 offset:36864
	ds_read_b128 v[198:201], v224 offset:38912
	s_mov_b32 m0, s62
	s_nop 0
	global_load_lds_dwordx4 v212, s[54:55] offset:0
	s_nop 0
	s_mov_b32 m0, s63
	s_nop 0
	global_load_lds_dwordx4 v214, s[54:55] offset:0
	s_waitcnt vmcnt(8)
	s_waitcnt lgkmcnt(0)
	s_barrier
	s_setprio 1
	s_waitcnt lgkmcnt(7)
	v_mfma_f32_16x16x32_bf16 v[126:129], v[130:133], v[166:169], v[126:129]
	v_mfma_f32_16x16x32_bf16 v[122:125], v[134:137], v[166:169], v[122:125]
	s_waitcnt lgkmcnt(6)
	v_mfma_f32_16x16x32_bf16 v[118:121], v[130:133], v[170:173], v[118:121]
	v_mfma_f32_16x16x32_bf16 v[114:117], v[134:137], v[170:173], v[114:117]
	s_waitcnt lgkmcnt(3)
	v_mfma_f32_16x16x32_bf16 v[110:113], v[130:133], v[182:185], v[110:113]
	v_mfma_f32_16x16x32_bf16 v[106:109], v[134:137], v[182:185], v[106:109]
	s_waitcnt lgkmcnt(2)
	v_mfma_f32_16x16x32_bf16 v[102:105], v[130:133], v[186:189], v[102:105]
	v_mfma_f32_16x16x32_bf16 v[98:101], v[134:137], v[186:189], v[98:101]
	v_mfma_f32_16x16x32_bf16 v[126:129], v[138:141], v[174:177], v[126:129]
	v_mfma_f32_16x16x32_bf16 v[122:125], v[142:145], v[174:177], v[122:125]
	v_mfma_f32_16x16x32_bf16 v[118:121], v[138:141], v[178:181], v[118:121]
	v_mfma_f32_16x16x32_bf16 v[114:117], v[142:145], v[178:181], v[114:117]
	s_waitcnt lgkmcnt(1)
	v_mfma_f32_16x16x32_bf16 v[110:113], v[138:141], v[190:193], v[110:113]
	v_mfma_f32_16x16x32_bf16 v[106:109], v[142:145], v[190:193], v[106:109]
	s_waitcnt lgkmcnt(0)
	v_mfma_f32_16x16x32_bf16 v[102:105], v[138:141], v[198:201], v[102:105]
	v_mfma_f32_16x16x32_bf16 v[98:101], v[142:145], v[198:201], v[98:101]
	s_setprio 0
	s_setprio 1
	v_mfma_f32_16x16x32_bf16 v[94:97], v[146:149], v[166:169], v[94:97]
	v_mfma_f32_16x16x32_bf16 v[90:93], v[150:153], v[166:169], v[90:93]
	v_mfma_f32_16x16x32_bf16 v[86:89], v[146:149], v[170:173], v[86:89]
	v_mfma_f32_16x16x32_bf16 v[82:85], v[150:153], v[170:173], v[82:85]
	v_mfma_f32_16x16x32_bf16 v[78:81], v[146:149], v[182:185], v[78:81]
	v_mfma_f32_16x16x32_bf16 v[74:77], v[150:153], v[182:185], v[74:77]
	v_mfma_f32_16x16x32_bf16 v[70:73], v[146:149], v[186:189], v[70:73]
	v_mfma_f32_16x16x32_bf16 v[66:69], v[150:153], v[186:189], v[66:69]
	v_mfma_f32_16x16x32_bf16 v[94:97], v[154:157], v[174:177], v[94:97]
	v_mfma_f32_16x16x32_bf16 v[90:93], v[158:161], v[174:177], v[90:93]
	v_mfma_f32_16x16x32_bf16 v[86:89], v[154:157], v[178:181], v[86:89]
	v_mfma_f32_16x16x32_bf16 v[82:85], v[158:161], v[178:181], v[82:85]
	v_mfma_f32_16x16x32_bf16 v[78:81], v[154:157], v[190:193], v[78:81]
	v_mfma_f32_16x16x32_bf16 v[74:77], v[158:161], v[190:193], v[74:77]
	v_mfma_f32_16x16x32_bf16 v[70:73], v[154:157], v[198:201], v[70:73]
	v_mfma_f32_16x16x32_bf16 v[66:69], v[158:161], v[198:201], v[66:69]
	s_setprio 0
	s_barrier
	ds_read_b128 v[166:169], v223 offset:49152
	ds_read_b128 v[170:173], v223 offset:51200
	ds_read_b128 v[174:177], v224 offset:49152
	ds_read_b128 v[178:181], v224 offset:51200
	ds_read_b128 v[182:185], v223 offset:53248
	ds_read_b128 v[186:189], v223 offset:55296
	ds_read_b128 v[190:193], v224 offset:53248
	ds_read_b128 v[198:201], v224 offset:55296
	s_add_u32 s54, s51, 0x180
	s_addc_u32 s55, s53, 0
	s_mov_b32 m0, s64
	s_nop 0
	global_load_lds_dwordx4 v215, s[54:55] offset:0
	s_nop 0
	s_mov_b32 m0, s65
	s_nop 0
	global_load_lds_dwordx4 v216, s[54:55] offset:0
	s_add_u32 s54, s51, 0x40180
	s_addc_u32 s55, s53, 0
	s_mov_b32 m0, s68
	s_nop 0
	global_load_lds_dwordx4 v215, s[54:55] offset:0
	s_nop 0
	s_mov_b32 m0, s69
	s_nop 0
	global_load_lds_dwordx4 v216, s[54:55] offset:0
	s_add_u32 s54, s47, 0x180
	s_addc_u32 s55, s50, 0
	s_mov_b32 m0, s66
	s_nop 0
	global_load_lds_dwordx4 v211, s[54:55] offset:0
	s_nop 0
	s_mov_b32 m0, s67
	s_nop 0
	global_load_lds_dwordx4 v213, s[54:55] offset:0
	s_waitcnt vmcnt(8)
	s_waitcnt lgkmcnt(0)
	s_barrier
	s_setprio 1
	s_waitcnt lgkmcnt(7)
	v_mfma_f32_16x16x32_bf16 v[62:65], v[130:133], v[166:169], v[62:65]
	v_mfma_f32_16x16x32_bf16 v[58:61], v[134:137], v[166:169], v[58:61]
	s_waitcnt lgkmcnt(6)
	v_mfma_f32_16x16x32_bf16 v[54:57], v[130:133], v[170:173], v[54:57]
	v_mfma_f32_16x16x32_bf16 v[50:53], v[134:137], v[170:173], v[50:53]
	s_waitcnt lgkmcnt(3)
	v_mfma_f32_16x16x32_bf16 v[46:49], v[130:133], v[182:185], v[46:49]
	v_mfma_f32_16x16x32_bf16 v[42:45], v[134:137], v[182:185], v[42:45]
	s_waitcnt lgkmcnt(2)
	v_mfma_f32_16x16x32_bf16 v[38:41], v[130:133], v[186:189], v[38:41]
	v_mfma_f32_16x16x32_bf16 v[34:37], v[134:137], v[186:189], v[34:37]
	v_mfma_f32_16x16x32_bf16 v[62:65], v[138:141], v[174:177], v[62:65]
	v_mfma_f32_16x16x32_bf16 v[58:61], v[142:145], v[174:177], v[58:61]
	v_mfma_f32_16x16x32_bf16 v[54:57], v[138:141], v[178:181], v[54:57]
	v_mfma_f32_16x16x32_bf16 v[50:53], v[142:145], v[178:181], v[50:53]
	s_waitcnt lgkmcnt(1)
	v_mfma_f32_16x16x32_bf16 v[46:49], v[138:141], v[190:193], v[46:49]
	v_mfma_f32_16x16x32_bf16 v[42:45], v[142:145], v[190:193], v[42:45]
	s_waitcnt lgkmcnt(0)
	v_mfma_f32_16x16x32_bf16 v[38:41], v[138:141], v[198:201], v[38:41]
	v_mfma_f32_16x16x32_bf16 v[34:37], v[142:145], v[198:201], v[34:37]
	s_setprio 0
	s_setprio 1
	v_mfma_f32_16x16x32_bf16 v[30:33], v[146:149], v[166:169], v[30:33]
	v_mfma_f32_16x16x32_bf16 v[26:29], v[150:153], v[166:169], v[26:29]
	v_mfma_f32_16x16x32_bf16 v[22:25], v[146:149], v[170:173], v[22:25]
	v_mfma_f32_16x16x32_bf16 v[18:21], v[150:153], v[170:173], v[18:21]
	v_mfma_f32_16x16x32_bf16 v[14:17], v[146:149], v[182:185], v[14:17]
	v_mfma_f32_16x16x32_bf16 v[10:13], v[150:153], v[182:185], v[10:13]
	v_mfma_f32_16x16x32_bf16 v[6:9], v[146:149], v[186:189], v[6:9]
	v_mfma_f32_16x16x32_bf16 v[2:5], v[150:153], v[186:189], v[2:5]
	v_mfma_f32_16x16x32_bf16 v[30:33], v[154:157], v[174:177], v[30:33]
	v_mfma_f32_16x16x32_bf16 v[26:29], v[158:161], v[174:177], v[26:29]
	v_mfma_f32_16x16x32_bf16 v[22:25], v[154:157], v[178:181], v[22:25]
	v_mfma_f32_16x16x32_bf16 v[18:21], v[158:161], v[178:181], v[18:21]
	v_mfma_f32_16x16x32_bf16 v[14:17], v[154:157], v[190:193], v[14:17]
	v_mfma_f32_16x16x32_bf16 v[10:13], v[158:161], v[190:193], v[10:13]
	v_mfma_f32_16x16x32_bf16 v[6:9], v[154:157], v[198:201], v[6:9]
	v_mfma_f32_16x16x32_bf16 v[2:5], v[158:161], v[198:201], v[2:5]
	s_setprio 0
	s_add_i32 s9, s9, 2
	s_add_u32 s4, s4, 0x100
	s_addc_u32 s5, s5, 0
	s_barrier
	.p2align 6

.LBB0_249:
	v_mov_b32_e32 v121, v120
	s_add_i32 s1, s68, 0x100
	v_pk_fma_f32 v[154:155], v[66:67], s[84:85], v[120:121] op_sel_hi:[1,0,1]
	v_mul_f32_e32 v67, 0, v179
	s_cmp_lg_u32 0, -1
	v_cndmask_b32_e64 v67, v67, 0, s[4:5]
	s_cselect_b32 s4, 0, 0
	v_add_f32_e32 v66, v114, v115
	s_add_i32 s86, s86, s4
	s_waitcnt vmcnt(0)
	v_mov_b32_e32 v82, v120
	v_mov_b32_e32 v83, v120
	v_add_f32_e32 v66, v67, v66
	v_add_f32_e32 v180, v116, v117
	s_add_i32 s87, s86, 0x2000
	v_pk_fma_f32 v[140:141], v[80:81], s[84:85], v[82:83] op_sel_hi:[1,0,1]
	v_pk_fma_f32 v[142:143], v[78:79], s[84:85], v[82:83] op_sel_hi:[1,0,1]
	v_pk_fma_f32 v[144:145], v[76:77], s[84:85], v[82:83] op_sel_hi:[1,0,1]
	v_pk_fma_f32 v[146:147], v[74:75], s[84:85], v[82:83] op_sel_hi:[1,0,1]
	v_pk_fma_f32 v[148:149], v[72:73], s[84:85], v[82:83] op_sel_hi:[1,0,1]
	v_pk_fma_f32 v[150:151], v[70:71], s[84:85], v[82:83] op_sel_hi:[1,0,1]
	v_pk_fma_f32 v[152:153], v[68:69], s[84:85], v[82:83] op_sel_hi:[1,0,1]
	v_fmac_f32_e32 v180, v66, v182
	s_cmp_lt_i32 s68, 64
	v_lshl_add_u32 v179, v138, 2, s80
	s_barrier
	s_cbranch_scc1 .LBB0_277
	s_add_i32 s6, s77, 0xffffff40
	v_add_u32_e32 v66, s6, v165
	s_lshr_b32 s94, s1, 6
	v_cmp_gt_u32_e64 s[4:5], 32, v163
	v_lshl_add_u32 v182, v165, 2, s80
	v_sub_u32_e32 v183, v66, v138
	s_movk_i32 s95, 0x1bf
	s_mov_b64 s[70:71], 0
	s_mov_b32 s75, 4
	.p2align 6

.LBB0_367:
	s_mov_b32 s31, -2
	s_mov_b64 s[6:7], 0
	.p2align 3
	s_nop 0
	ds_read_b128 v[130:133], v203
	ds_read_b128 v[134:137], v203 offset:2048
	ds_read_b128 v[138:141], v204
	ds_read_b128 v[142:145], v204 offset:2048
	ds_read_b128 v[146:149], v205
	ds_read_b128 v[150:153], v205 offset:2048
	ds_read_b128 v[154:157], v206
	ds_read_b128 v[158:161], v206 offset:2048
	ds_read_b128 v[162:165], v207
	ds_read_b128 v[166:169], v207 offset:2048
	ds_read_b128 v[174:177], v208
	ds_read_b128 v[178:181], v208 offset:2048
	ds_read_b128 v[182:185], v207 offset:4096
	ds_read_b128 v[210:213], v207 offset:6144
	ds_read_b128 v[214:217], v208 offset:4096
	ds_read_b128 v[218:221], v208 offset:6144
	s_add_u32 s36, s8, s6
	s_addc_u32 s37, s9, s7
	s_add_u32 s58, s36, 0x80
	s_addc_u32 s59, s37, 0
	s_mov_b32 m0, s52
	s_nop 0
	global_load_lds_dwordx4 v198, s[58:59] offset:0
	s_nop 0
	s_mov_b32 m0, s53
	s_nop 0
	global_load_lds_dwordx4 v200, s[58:59] offset:0
	s_waitcnt vmcnt(8)
	s_waitcnt lgkmcnt(0)
	s_barrier
	s_setprio 1
	s_waitcnt lgkmcnt(7)
	v_mfma_f32_16x16x32_bf16 v[126:129], v[130:133], v[162:165], 0
	v_mfma_f32_16x16x32_bf16 v[122:125], v[134:137], v[162:165], 0
	s_waitcnt lgkmcnt(6)
	v_mfma_f32_16x16x32_bf16 v[118:121], v[130:133], v[166:169], 0
	v_mfma_f32_16x16x32_bf16 v[114:117], v[134:137], v[166:169], 0
	s_waitcnt lgkmcnt(3)
	v_mfma_f32_16x16x32_bf16 v[110:113], v[130:133], v[182:185], 0
	v_mfma_f32_16x16x32_bf16 v[106:109], v[134:137], v[182:185], 0
	s_waitcnt lgkmcnt(2)
	v_mfma_f32_16x16x32_bf16 v[102:105], v[130:133], v[210:213], 0
	v_mfma_f32_16x16x32_bf16 v[98:101], v[134:137], v[210:213], 0
	v_mfma_f32_16x16x32_bf16 v[126:129], v[138:141], v[174:177], v[126:129]
	v_mfma_f32_16x16x32_bf16 v[122:125], v[142:145], v[174:177], v[122:125]
	v_mfma_f32_16x16x32_bf16 v[118:121], v[138:141], v[178:181], v[118:121]
	v_mfma_f32_16x16x32_bf16 v[114:117], v[142:145], v[178:181], v[114:117]
	s_waitcnt lgkmcnt(1)
	v_mfma_f32_16x16x32_bf16 v[110:113], v[138:141], v[214:217], v[110:113]
	v_mfma_f32_16x16x32_bf16 v[106:109], v[142:145], v[214:217], v[106:109]
	s_waitcnt lgkmcnt(0)
	v_mfma_f32_16x16x32_bf16 v[102:105], v[138:141], v[218:221], v[102:105]
	v_mfma_f32_16x16x32_bf16 v[98:101], v[142:145], v[218:221], v[98:101]
	s_setprio 0
	s_setprio 1
	v_mfma_f32_16x16x32_bf16 v[94:97], v[146:149], v[162:165], 0
	v_mfma_f32_16x16x32_bf16 v[90:93], v[150:153], v[162:165], 0
	v_mfma_f32_16x16x32_bf16 v[86:89], v[146:149], v[166:169], 0
	v_mfma_f32_16x16x32_bf16 v[82:85], v[150:153], v[166:169], 0
	v_mfma_f32_16x16x32_bf16 v[78:81], v[146:149], v[182:185], 0
	v_mfma_f32_16x16x32_bf16 v[74:77], v[150:153], v[182:185], 0
	v_mfma_f32_16x16x32_bf16 v[70:73], v[146:149], v[210:213], 0
	v_mfma_f32_16x16x32_bf16 v[66:69], v[150:153], v[210:213], 0
	v_mfma_f32_16x16x32_bf16 v[94:97], v[154:157], v[174:177], v[94:97]
	v_mfma_f32_16x16x32_bf16 v[90:93], v[158:161], v[174:177], v[90:93]
	v_mfma_f32_16x16x32_bf16 v[86:89], v[154:157], v[178:181], v[86:89]
	v_mfma_f32_16x16x32_bf16 v[82:85], v[158:161], v[178:181], v[82:85]
	v_mfma_f32_16x16x32_bf16 v[78:81], v[154:157], v[214:217], v[78:81]
	v_mfma_f32_16x16x32_bf16 v[74:77], v[158:161], v[214:217], v[74:77]
	v_mfma_f32_16x16x32_bf16 v[70:73], v[154:157], v[218:221], v[70:73]
	v_mfma_f32_16x16x32_bf16 v[66:69], v[158:161], v[218:221], v[66:69]
	s_setprio 0
	s_barrier
	s_add_u32 s60, s34, s6
	s_addc_u32 s61, s35, s7
	ds_read_b128 v[162:165], v207 offset:16384
	ds_read_b128 v[166:169], v207 offset:18432
	ds_read_b128 v[174:177], v208 offset:16384
	ds_read_b128 v[178:181], v208 offset:18432
	ds_read_b128 v[182:185], v207 offset:20480
	ds_read_b128 v[210:213], v207 offset:22528
	ds_read_b128 v[214:217], v208 offset:20480
	ds_read_b128 v[218:221], v208 offset:22528
	s_add_u32 s58, s60, 0x100
	s_addc_u32 s59, s61, 0
	s_mov_b32 m0, s39
	s_nop 0
	global_load_lds_dwordx4 v195, s[58:59] offset:0
	s_nop 0
	s_mov_b32 m0, s40
	s_nop 0
	global_load_lds_dwordx4 v196, s[58:59] offset:0
	s_add_u32 s58, s60, 0x40100
	s_addc_u32 s59, s61, 0
	s_mov_b32 m0, s41
	s_nop 0
	global_load_lds_dwordx4 v195, s[58:59] offset:0
	s_nop 0
	s_mov_b32 m0, s42
	s_nop 0
	global_load_lds_dwordx4 v196, s[58:59] offset:0
	s_add_u32 s58, s36, 0x100
	s_addc_u32 s59, s37, 0
	s_mov_b32 m0, s38
	s_nop 0
	global_load_lds_dwordx4 v197, s[58:59] offset:0
	s_nop 0
	s_mov_b32 m0, s43
	s_nop 0
	global_load_lds_dwordx4 v199, s[58:59] offset:0
	s_waitcnt vmcnt(8)
	s_waitcnt lgkmcnt(0)
	s_barrier
	s_setprio 1
	s_waitcnt lgkmcnt(7)
	v_mfma_f32_16x16x32_bf16 v[62:65], v[130:133], v[162:165], 0
	v_mfma_f32_16x16x32_bf16 v[58:61], v[134:137], v[162:165], 0
	s_waitcnt lgkmcnt(6)
	v_mfma_f32_16x16x32_bf16 v[54:57], v[130:133], v[166:169], 0
	v_mfma_f32_16x16x32_bf16 v[50:53], v[134:137], v[166:169], 0
	s_waitcnt lgkmcnt(3)
	v_mfma_f32_16x16x32_bf16 v[46:49], v[130:133], v[182:185], 0
	v_mfma_f32_16x16x32_bf16 v[42:45], v[134:137], v[182:185], 0
	s_waitcnt lgkmcnt(2)
	v_mfma_f32_16x16x32_bf16 v[38:41], v[130:133], v[210:213], 0
	v_mfma_f32_16x16x32_bf16 v[34:37], v[134:137], v[210:213], 0
	v_mfma_f32_16x16x32_bf16 v[62:65], v[138:141], v[174:177], v[62:65]
	v_mfma_f32_16x16x32_bf16 v[58:61], v[142:145], v[174:177], v[58:61]
	v_mfma_f32_16x16x32_bf16 v[54:57], v[138:141], v[178:181], v[54:57]
	v_mfma_f32_16x16x32_bf16 v[50:53], v[142:145], v[178:181], v[50:53]
	s_waitcnt lgkmcnt(1)
	v_mfma_f32_16x16x32_bf16 v[46:49], v[138:141], v[214:217], v[46:49]
	v_mfma_f32_16x16x32_bf16 v[42:45], v[142:145], v[214:217], v[42:45]
	s_waitcnt lgkmcnt(0)
	v_mfma_f32_16x16x32_bf16 v[38:41], v[138:141], v[218:221], v[38:41]
	v_mfma_f32_16x16x32_bf16 v[34:37], v[142:145], v[218:221], v[34:37]
	s_setprio 0
	s_setprio 1
	v_mfma_f32_16x16x32_bf16 v[30:33], v[146:149], v[162:165], 0
	v_mfma_f32_16x16x32_bf16 v[26:29], v[150:153], v[162:165], 0
	v_mfma_f32_16x16x32_bf16 v[22:25], v[146:149], v[166:169], 0
	v_mfma_f32_16x16x32_bf16 v[18:21], v[150:153], v[166:169], 0
	v_mfma_f32_16x16x32_bf16 v[14:17], v[146:149], v[182:185], 0
	v_mfma_f32_16x16x32_bf16 v[10:13], v[150:153], v[182:185], 0
	v_mfma_f32_16x16x32_bf16 v[6:9], v[146:149], v[210:213], 0
	v_mfma_f32_16x16x32_bf16 v[2:5], v[150:153], v[210:213], 0
	v_mfma_f32_16x16x32_bf16 v[30:33], v[154:157], v[174:177], v[30:33]
	v_mfma_f32_16x16x32_bf16 v[26:29], v[158:161], v[174:177], v[26:29]
	v_mfma_f32_16x16x32_bf16 v[22:25], v[154:157], v[178:181], v[22:25]
	v_mfma_f32_16x16x32_bf16 v[18:21], v[158:161], v[178:181], v[18:21]
	v_mfma_f32_16x16x32_bf16 v[14:17], v[154:157], v[214:217], v[14:17]
	v_mfma_f32_16x16x32_bf16 v[10:13], v[158:161], v[214:217], v[10:13]
	v_mfma_f32_16x16x32_bf16 v[6:9], v[154:157], v[218:221], v[6:9]
	v_mfma_f32_16x16x32_bf16 v[2:5], v[158:161], v[218:221], v[2:5]
	s_setprio 0
	s_barrier
	s_add_i32 s62, 0, 0x18000
	v_add_u32_e32 v174, s62, v201
	v_add_u32_e32 v175, s62, v202
	s_add_i32 s62, 0, 0x1c000
	v_add_u32_e32 v176, s62, v201
	ds_read_b128 v[130:133], v174
	ds_read_b128 v[134:137], v174 offset:2048
	ds_read_b128 v[138:141], v175
	ds_read_b128 v[142:145], v175 offset:2048
	v_add_u32_e32 v177, s62, v202
	ds_read_b128 v[146:149], v176
	ds_read_b128 v[150:153], v176 offset:2048
	ds_read_b128 v[154:157], v177
	ds_read_b128 v[158:161], v177 offset:2048
	ds_read_b128 v[162:165], v207 offset:32768
	ds_read_b128 v[166:169], v207 offset:34816
	ds_read_b128 v[178:181], v208 offset:32768
	ds_read_b128 v[182:185], v208 offset:34816
	ds_read_b128 v[210:213], v207 offset:36864
	ds_read_b128 v[214:217], v207 offset:38912
	ds_read_b128 v[218:221], v208 offset:36864
	ds_read_b128 v[222:225], v208 offset:38912
	s_mov_b32 m0, s44
	s_nop 0
	global_load_lds_dwordx4 v198, s[58:59] offset:0
	s_nop 0
	s_mov_b32 m0, s45
	s_nop 0
	global_load_lds_dwordx4 v200, s[58:59] offset:0
	s_waitcnt vmcnt(8)
	s_waitcnt lgkmcnt(0)
	s_barrier
	s_setprio 1
	s_waitcnt lgkmcnt(7)
	v_mfma_f32_16x16x32_bf16 v[126:129], v[130:133], v[162:165], v[126:129]
	v_mfma_f32_16x16x32_bf16 v[122:125], v[134:137], v[162:165], v[122:125]
	s_waitcnt lgkmcnt(6)
	v_mfma_f32_16x16x32_bf16 v[118:121], v[130:133], v[166:169], v[118:121]
	v_mfma_f32_16x16x32_bf16 v[114:117], v[134:137], v[166:169], v[114:117]
	s_waitcnt lgkmcnt(3)
	v_mfma_f32_16x16x32_bf16 v[110:113], v[130:133], v[210:213], v[110:113]
	v_mfma_f32_16x16x32_bf16 v[106:109], v[134:137], v[210:213], v[106:109]
	s_waitcnt lgkmcnt(2)
	v_mfma_f32_16x16x32_bf16 v[102:105], v[130:133], v[214:217], v[102:105]
	v_mfma_f32_16x16x32_bf16 v[98:101], v[134:137], v[214:217], v[98:101]
	v_mfma_f32_16x16x32_bf16 v[126:129], v[138:141], v[178:181], v[126:129]
	v_mfma_f32_16x16x32_bf16 v[122:125], v[142:145], v[178:181], v[122:125]
	v_mfma_f32_16x16x32_bf16 v[118:121], v[138:141], v[182:185], v[118:121]
	v_mfma_f32_16x16x32_bf16 v[114:117], v[142:145], v[182:185], v[114:117]
	s_waitcnt lgkmcnt(1)
	v_mfma_f32_16x16x32_bf16 v[110:113], v[138:141], v[218:221], v[110:113]
	v_mfma_f32_16x16x32_bf16 v[106:109], v[142:145], v[218:221], v[106:109]
	s_waitcnt lgkmcnt(0)
	v_mfma_f32_16x16x32_bf16 v[102:105], v[138:141], v[222:225], v[102:105]
	v_mfma_f32_16x16x32_bf16 v[98:101], v[142:145], v[222:225], v[98:101]
	s_setprio 0
	s_setprio 1
	v_mfma_f32_16x16x32_bf16 v[94:97], v[146:149], v[162:165], v[94:97]
	v_mfma_f32_16x16x32_bf16 v[90:93], v[150:153], v[162:165], v[90:93]
	v_mfma_f32_16x16x32_bf16 v[86:89], v[146:149], v[166:169], v[86:89]
	v_mfma_f32_16x16x32_bf16 v[82:85], v[150:153], v[166:169], v[82:85]
	v_mfma_f32_16x16x32_bf16 v[78:81], v[146:149], v[210:213], v[78:81]
	v_mfma_f32_16x16x32_bf16 v[74:77], v[150:153], v[210:213], v[74:77]
	v_mfma_f32_16x16x32_bf16 v[70:73], v[146:149], v[214:217], v[70:73]
	v_mfma_f32_16x16x32_bf16 v[66:69], v[150:153], v[214:217], v[66:69]
	v_mfma_f32_16x16x32_bf16 v[94:97], v[154:157], v[178:181], v[94:97]
	v_mfma_f32_16x16x32_bf16 v[90:93], v[158:161], v[178:181], v[90:93]
	v_mfma_f32_16x16x32_bf16 v[86:89], v[154:157], v[182:185], v[86:89]
	v_mfma_f32_16x16x32_bf16 v[82:85], v[158:161], v[182:185], v[82:85]
	v_mfma_f32_16x16x32_bf16 v[78:81], v[154:157], v[218:221], v[78:81]
	v_mfma_f32_16x16x32_bf16 v[74:77], v[158:161], v[218:221], v[74:77]
	v_mfma_f32_16x16x32_bf16 v[70:73], v[154:157], v[222:225], v[70:73]
	v_mfma_f32_16x16x32_bf16 v[66:69], v[158:161], v[222:225], v[66:69]
	s_setprio 0
	s_barrier
	ds_read_b128 v[162:165], v207 offset:49152
	ds_read_b128 v[166:169], v207 offset:51200
	ds_read_b128 v[178:181], v208 offset:49152
	ds_read_b128 v[182:185], v208 offset:51200
	ds_read_b128 v[210:213], v207 offset:53248
	ds_read_b128 v[214:217], v207 offset:55296
	ds_read_b128 v[218:221], v208 offset:53248
	ds_read_b128 v[222:225], v208 offset:55296
	s_add_u32 s58, s60, 0x180
	s_addc_u32 s59, s61, 0
	s_mov_b32 m0, s46
	s_nop 0
	global_load_lds_dwordx4 v195, s[58:59] offset:0
	s_nop 0
	s_mov_b32 m0, s47
	s_nop 0
	global_load_lds_dwordx4 v196, s[58:59] offset:0
	s_add_u32 s58, s60, 0x40180
	s_addc_u32 s59, s61, 0
	s_mov_b32 m0, s50
	s_nop 0
	global_load_lds_dwordx4 v195, s[58:59] offset:0
	s_add_u32 s36, s36, 0x180
	s_mov_b32 m0, s51
	s_nop 0
	global_load_lds_dwordx4 v196, s[58:59] offset:0
	s_addc_u32 s37, s37, 0
	s_mov_b32 m0, s48
	s_nop 0
	global_load_lds_dwordx4 v197, s[36:37] offset:0
	s_nop 0
	s_mov_b32 m0, s49
	s_nop 0
	global_load_lds_dwordx4 v199, s[36:37] offset:0
	s_waitcnt vmcnt(8)
	s_waitcnt lgkmcnt(0)
	s_barrier
	s_setprio 1
	s_waitcnt lgkmcnt(7)
	v_mfma_f32_16x16x32_bf16 v[62:65], v[130:133], v[162:165], v[62:65]
	v_mfma_f32_16x16x32_bf16 v[58:61], v[134:137], v[162:165], v[58:61]
	s_waitcnt lgkmcnt(6)
	v_mfma_f32_16x16x32_bf16 v[54:57], v[130:133], v[166:169], v[54:57]
	v_mfma_f32_16x16x32_bf16 v[50:53], v[134:137], v[166:169], v[50:53]
	s_waitcnt lgkmcnt(3)
	v_mfma_f32_16x16x32_bf16 v[46:49], v[130:133], v[210:213], v[46:49]
	v_mfma_f32_16x16x32_bf16 v[42:45], v[134:137], v[210:213], v[42:45]
	s_waitcnt lgkmcnt(2)
	v_mfma_f32_16x16x32_bf16 v[38:41], v[130:133], v[214:217], v[38:41]
	v_mfma_f32_16x16x32_bf16 v[34:37], v[134:137], v[214:217], v[34:37]
	v_mfma_f32_16x16x32_bf16 v[62:65], v[138:141], v[178:181], v[62:65]
	v_mfma_f32_16x16x32_bf16 v[58:61], v[142:145], v[178:181], v[58:61]
	v_mfma_f32_16x16x32_bf16 v[54:57], v[138:141], v[182:185], v[54:57]
	v_mfma_f32_16x16x32_bf16 v[50:53], v[142:145], v[182:185], v[50:53]
	s_waitcnt lgkmcnt(1)
	v_mfma_f32_16x16x32_bf16 v[46:49], v[138:141], v[218:221], v[46:49]
	v_mfma_f32_16x16x32_bf16 v[42:45], v[142:145], v[218:221], v[42:45]
	s_waitcnt lgkmcnt(0)
	v_mfma_f32_16x16x32_bf16 v[38:41], v[138:141], v[222:225], v[38:41]
	v_mfma_f32_16x16x32_bf16 v[34:37], v[142:145], v[222:225], v[34:37]
	s_setprio 0
	s_setprio 1
	v_mfma_f32_16x16x32_bf16 v[30:33], v[146:149], v[162:165], v[30:33]
	v_mfma_f32_16x16x32_bf16 v[26:29], v[150:153], v[162:165], v[26:29]
	v_mfma_f32_16x16x32_bf16 v[22:25], v[146:149], v[166:169], v[22:25]
	v_mfma_f32_16x16x32_bf16 v[18:21], v[150:153], v[166:169], v[18:21]
	v_mfma_f32_16x16x32_bf16 v[14:17], v[146:149], v[210:213], v[14:17]
	v_mfma_f32_16x16x32_bf16 v[10:13], v[150:153], v[210:213], v[10:13]
	v_mfma_f32_16x16x32_bf16 v[6:9], v[146:149], v[214:217], v[6:9]
	v_mfma_f32_16x16x32_bf16 v[2:5], v[150:153], v[214:217], v[2:5]
	v_mfma_f32_16x16x32_bf16 v[30:33], v[154:157], v[178:181], v[30:33]
	v_mfma_f32_16x16x32_bf16 v[26:29], v[158:161], v[178:181], v[26:29]
	v_mfma_f32_16x16x32_bf16 v[22:25], v[154:157], v[182:185], v[22:25]
	v_mfma_f32_16x16x32_bf16 v[18:21], v[158:161], v[182:185], v[18:21]
	v_mfma_f32_16x16x32_bf16 v[14:17], v[154:157], v[218:221], v[14:17]
	v_mfma_f32_16x16x32_bf16 v[10:13], v[158:161], v[218:221], v[10:13]
	v_mfma_f32_16x16x32_bf16 v[6:9], v[154:157], v[222:225], v[6:9]
	v_mfma_f32_16x16x32_bf16 v[2:5], v[158:161], v[222:225], v[2:5]
	s_setprio 0
	s_add_i32 s31, s31, 2
	s_add_u32 s6, s6, 0x100
	s_addc_u32 s7, s7, 0
	s_barrier
	.p2align 6

.LBB0_560:
	s_mov_b32 s35, -2
	.p2align 3
	s_nop 0
	ds_read_b128 v[18:21], v179
	ds_read_b128 v[26:29], v179 offset:2048
	ds_read_b128 v[22:25], v180
	ds_read_b128 v[30:33], v180 offset:2048
	ds_read_b128 v[2:5], v181
	ds_read_b128 v[10:13], v181 offset:2048
	ds_read_b128 v[6:9], v182
	ds_read_b128 v[14:17], v182 offset:2048
	ds_read_b128 v[194:197], v183
	ds_read_b128 v[202:205], v183 offset:2048
	ds_read_b128 v[198:201], v184
	ds_read_b128 v[206:209], v184 offset:2048
	ds_read_b128 v[210:213], v183 offset:4096
	ds_read_b128 v[218:221], v183 offset:6144
	ds_read_b128 v[214:217], v184 offset:4096
	ds_read_b128 v[222:225], v184 offset:6144
	s_add_u32 s39, s18, s4
	s_addc_u32 s68, s19, s5
	s_add_u32 s42, s39, 0x80
	s_addc_u32 s43, s68, 0
	s_mov_b32 m0, s61
	s_nop 0
	global_load_lds_dwordx4 v172, s[42:43] offset:0
	s_nop 0
	s_mov_b32 m0, s62
	s_nop 0
	global_load_lds_dwordx4 v175, s[42:43] offset:0
	s_waitcnt vmcnt(8)
	s_waitcnt lgkmcnt(0)
	s_barrier
	s_setprio 1
	s_waitcnt lgkmcnt(5)
	v_mfma_f32_16x16x128_f8f6f4 v[158:161], v[18:25], v[194:201], 0
	v_mfma_f32_16x16x128_f8f6f4 v[150:153], v[26:33], v[194:201], 0
	s_waitcnt lgkmcnt(4)
	v_mfma_f32_16x16x128_f8f6f4 v[142:145], v[18:25], v[202:209], 0
	v_mfma_f32_16x16x128_f8f6f4 v[134:137], v[26:33], v[202:209], 0
	s_waitcnt lgkmcnt(1)
	v_mfma_f32_16x16x128_f8f6f4 v[126:129], v[18:25], v[210:217], 0
	v_mfma_f32_16x16x128_f8f6f4 v[118:121], v[26:33], v[210:217], 0
	s_waitcnt lgkmcnt(0)
	v_mfma_f32_16x16x128_f8f6f4 v[110:113], v[18:25], v[218:225], 0
	v_mfma_f32_16x16x128_f8f6f4 v[102:105], v[26:33], v[218:225], 0
	s_setprio 0
	s_setprio 1
	v_mfma_f32_16x16x128_f8f6f4 v[154:157], v[2:9], v[194:201], 0
	v_mfma_f32_16x16x128_f8f6f4 v[146:149], v[10:17], v[194:201], 0
	v_mfma_f32_16x16x128_f8f6f4 v[138:141], v[2:9], v[202:209], 0
	v_mfma_f32_16x16x128_f8f6f4 v[130:133], v[10:17], v[202:209], 0
	v_mfma_f32_16x16x128_f8f6f4 v[122:125], v[2:9], v[210:217], 0
	v_mfma_f32_16x16x128_f8f6f4 v[114:117], v[10:17], v[210:217], 0
	v_mfma_f32_16x16x128_f8f6f4 v[106:109], v[2:9], v[218:225], 0
	v_mfma_f32_16x16x128_f8f6f4 v[98:101], v[10:17], v[218:225], 0
	s_setprio 0
	s_barrier
	s_add_u32 s69, s44, s4
	s_addc_u32 s70, s45, s5
	ds_read_b128 v[194:197], v183 offset:16384
	ds_read_b128 v[202:205], v183 offset:18432
	ds_read_b128 v[198:201], v184 offset:16384
	ds_read_b128 v[206:209], v184 offset:18432
	ds_read_b128 v[210:213], v183 offset:20480
	ds_read_b128 v[218:221], v183 offset:22528
	ds_read_b128 v[214:217], v184 offset:20480
	ds_read_b128 v[222:225], v184 offset:22528
	s_add_u32 s42, s69, 0x100
	s_addc_u32 s43, s70, 0
	s_mov_b32 m0, s48
	s_nop 0
	global_load_lds_dwordx4 v1, s[42:43] offset:0
	s_nop 0
	s_mov_b32 m0, s49
	s_nop 0
	global_load_lds_dwordx4 v173, s[42:43] offset:0
	s_add_u32 s42, s69, 0x20100
	s_addc_u32 s43, s70, 0
	s_mov_b32 m0, s50
	s_nop 0
	global_load_lds_dwordx4 v1, s[42:43] offset:0
	s_nop 0
	s_mov_b32 m0, s51
	s_nop 0
	global_load_lds_dwordx4 v173, s[42:43] offset:0
	s_add_u32 s42, s39, 0x100
	s_addc_u32 s43, s68, 0
	s_mov_b32 m0, s29
	s_nop 0
	global_load_lds_dwordx4 v171, s[42:43] offset:0
	s_nop 0
	s_mov_b32 m0, s52
	s_nop 0
	global_load_lds_dwordx4 v174, s[42:43] offset:0
	s_waitcnt vmcnt(8)
	s_waitcnt lgkmcnt(0)
	s_barrier
	s_setprio 1
	s_waitcnt lgkmcnt(5)
	v_mfma_f32_16x16x128_f8f6f4 v[94:97], v[18:25], v[194:201], 0
	v_mfma_f32_16x16x128_f8f6f4 v[86:89], v[26:33], v[194:201], 0
	s_waitcnt lgkmcnt(4)
	v_mfma_f32_16x16x128_f8f6f4 v[78:81], v[18:25], v[202:209], 0
	v_mfma_f32_16x16x128_f8f6f4 v[70:73], v[26:33], v[202:209], 0
	s_waitcnt lgkmcnt(1)
	v_mfma_f32_16x16x128_f8f6f4 v[62:65], v[18:25], v[210:217], 0
	v_mfma_f32_16x16x128_f8f6f4 v[54:57], v[26:33], v[210:217], 0
	s_waitcnt lgkmcnt(0)
	v_mfma_f32_16x16x128_f8f6f4 v[46:49], v[18:25], v[218:225], 0
	v_mfma_f32_16x16x128_f8f6f4 v[38:41], v[26:33], v[218:225], 0
	s_setprio 0
	s_setprio 1
	v_mfma_f32_16x16x128_f8f6f4 v[90:93], v[2:9], v[194:201], 0
	v_mfma_f32_16x16x128_f8f6f4 v[82:85], v[10:17], v[194:201], 0
	v_mfma_f32_16x16x128_f8f6f4 v[74:77], v[2:9], v[202:209], 0
	v_mfma_f32_16x16x128_f8f6f4 v[66:69], v[10:17], v[202:209], 0
	v_mfma_f32_16x16x128_f8f6f4 v[58:61], v[2:9], v[210:217], 0
	v_mfma_f32_16x16x128_f8f6f4 v[50:53], v[10:17], v[210:217], 0
	v_mfma_f32_16x16x128_f8f6f4 v[42:45], v[2:9], v[218:225], 0
	v_mfma_f32_16x16x128_f8f6f4 v[34:37], v[10:17], v[218:225], 0
	s_setprio 0
	s_barrier
	s_add_i32 s71, 0, 0x18000
	v_add_u32_e32 v162, s71, v176
	v_add_u32_e32 v187, s71, v177
	s_add_i32 s71, 0, 0x1c000
	v_add_u32_e32 v194, s71, v176
	ds_read_b128 v[2:5], v162
	ds_read_b128 v[10:13], v162 offset:2048
	ds_read_b128 v[6:9], v187
	ds_read_b128 v[14:17], v187 offset:2048
	v_add_u32_e32 v195, s71, v177
	ds_read_b128 v[18:21], v194
	ds_read_b128 v[26:29], v194 offset:2048
	ds_read_b128 v[22:25], v195
	ds_read_b128 v[30:33], v195 offset:2048
	ds_read_b128 v[196:199], v183 offset:32768
	ds_read_b128 v[204:207], v183 offset:34816
	ds_read_b128 v[200:203], v184 offset:32768
	ds_read_b128 v[208:211], v184 offset:34816
	ds_read_b128 v[212:215], v183 offset:36864
	ds_read_b128 v[220:223], v183 offset:38912
	ds_read_b128 v[216:219], v184 offset:36864
	ds_read_b128 v[224:227], v184 offset:38912
	s_mov_b32 m0, s53
	s_nop 0
	global_load_lds_dwordx4 v172, s[42:43] offset:0
	s_nop 0
	s_mov_b32 m0, s54
	s_nop 0
	global_load_lds_dwordx4 v175, s[42:43] offset:0
	s_waitcnt vmcnt(8)
	s_waitcnt lgkmcnt(0)
	s_barrier
	s_setprio 1
	s_waitcnt lgkmcnt(5)
	v_mfma_f32_16x16x128_f8f6f4 v[158:161], v[2:9], v[196:203], v[158:161]
	v_mfma_f32_16x16x128_f8f6f4 v[150:153], v[10:17], v[196:203], v[150:153]
	s_waitcnt lgkmcnt(4)
	v_mfma_f32_16x16x128_f8f6f4 v[142:145], v[2:9], v[204:211], v[142:145]
	v_mfma_f32_16x16x128_f8f6f4 v[134:137], v[10:17], v[204:211], v[134:137]
	s_waitcnt lgkmcnt(1)
	v_mfma_f32_16x16x128_f8f6f4 v[126:129], v[2:9], v[212:219], v[126:129]
	v_mfma_f32_16x16x128_f8f6f4 v[118:121], v[10:17], v[212:219], v[118:121]
	s_waitcnt lgkmcnt(0)
	v_mfma_f32_16x16x128_f8f6f4 v[110:113], v[2:9], v[220:227], v[110:113]
	v_mfma_f32_16x16x128_f8f6f4 v[102:105], v[10:17], v[220:227], v[102:105]
	s_setprio 0
	s_setprio 1
	v_mfma_f32_16x16x128_f8f6f4 v[154:157], v[18:25], v[196:203], v[154:157]
	v_mfma_f32_16x16x128_f8f6f4 v[146:149], v[26:33], v[196:203], v[146:149]
	v_mfma_f32_16x16x128_f8f6f4 v[138:141], v[18:25], v[204:211], v[138:141]
	v_mfma_f32_16x16x128_f8f6f4 v[130:133], v[26:33], v[204:211], v[130:133]
	v_mfma_f32_16x16x128_f8f6f4 v[122:125], v[18:25], v[212:219], v[122:125]
	v_mfma_f32_16x16x128_f8f6f4 v[114:117], v[26:33], v[212:219], v[114:117]
	v_mfma_f32_16x16x128_f8f6f4 v[106:109], v[18:25], v[220:227], v[106:109]
	v_mfma_f32_16x16x128_f8f6f4 v[98:101], v[26:33], v[220:227], v[98:101]
	s_setprio 0
	s_barrier
	ds_read_b128 v[196:199], v183 offset:49152
	ds_read_b128 v[204:207], v183 offset:51200
	ds_read_b128 v[200:203], v184 offset:49152
	ds_read_b128 v[208:211], v184 offset:51200
	ds_read_b128 v[212:215], v183 offset:53248
	ds_read_b128 v[220:223], v183 offset:55296
	ds_read_b128 v[216:219], v184 offset:53248
	ds_read_b128 v[224:227], v184 offset:55296
	s_add_u32 s42, s69, 0x180
	s_addc_u32 s43, s70, 0
	s_mov_b32 m0, s55
	s_nop 0
	global_load_lds_dwordx4 v1, s[42:43] offset:0
	s_nop 0
	s_mov_b32 m0, s56
	s_nop 0
	global_load_lds_dwordx4 v173, s[42:43] offset:0
	s_add_u32 s42, s69, 0x20180
	s_addc_u32 s43, s70, 0
	s_mov_b32 m0, s59
	s_nop 0
	global_load_lds_dwordx4 v1, s[42:43] offset:0
	s_nop 0
	s_mov_b32 m0, s60
	s_nop 0
	global_load_lds_dwordx4 v173, s[42:43] offset:0
	s_add_u32 s42, s39, 0x180
	s_addc_u32 s43, s68, 0
	s_mov_b32 m0, s57
	s_nop 0
	global_load_lds_dwordx4 v171, s[42:43] offset:0
	s_nop 0
	s_mov_b32 m0, s58
	s_nop 0
	global_load_lds_dwordx4 v174, s[42:43] offset:0
	s_waitcnt vmcnt(8)
	s_waitcnt lgkmcnt(0)
	s_barrier
	s_setprio 1
	s_waitcnt lgkmcnt(5)
	v_mfma_f32_16x16x128_f8f6f4 v[94:97], v[2:9], v[196:203], v[94:97]
	v_mfma_f32_16x16x128_f8f6f4 v[86:89], v[10:17], v[196:203], v[86:89]
	s_waitcnt lgkmcnt(4)
	v_mfma_f32_16x16x128_f8f6f4 v[78:81], v[2:9], v[204:211], v[78:81]
	v_mfma_f32_16x16x128_f8f6f4 v[70:73], v[10:17], v[204:211], v[70:73]
	s_waitcnt lgkmcnt(1)
	v_mfma_f32_16x16x128_f8f6f4 v[62:65], v[2:9], v[212:219], v[62:65]
	v_mfma_f32_16x16x128_f8f6f4 v[54:57], v[10:17], v[212:219], v[54:57]
	s_waitcnt lgkmcnt(0)
	v_mfma_f32_16x16x128_f8f6f4 v[46:49], v[2:9], v[220:227], v[46:49]
	v_mfma_f32_16x16x128_f8f6f4 v[38:41], v[10:17], v[220:227], v[38:41]
	s_setprio 0
	s_setprio 1
	v_mfma_f32_16x16x128_f8f6f4 v[90:93], v[18:25], v[196:203], v[90:93]
	v_mfma_f32_16x16x128_f8f6f4 v[82:85], v[26:33], v[196:203], v[82:85]
	v_mfma_f32_16x16x128_f8f6f4 v[74:77], v[18:25], v[204:211], v[74:77]
	v_mfma_f32_16x16x128_f8f6f4 v[66:69], v[26:33], v[204:211], v[66:69]
	v_mfma_f32_16x16x128_f8f6f4 v[58:61], v[18:25], v[212:219], v[58:61]
	v_mfma_f32_16x16x128_f8f6f4 v[50:53], v[26:33], v[212:219], v[50:53]
	v_mfma_f32_16x16x128_f8f6f4 v[42:45], v[18:25], v[220:227], v[42:45]
	v_mfma_f32_16x16x128_f8f6f4 v[34:37], v[26:33], v[220:227], v[34:37]
	s_setprio 0
	s_add_i32 s35, s35, 2
	s_add_u32 s4, s4, 0x100
	s_addc_u32 s5, s5, 0
	s_barrier
	.p2align 6

.LBB0_649:
	s_mov_b32 s35, -2
	.p2align 3
	s_nop 0
	ds_read_b128 v[18:21], v176
	ds_read_b128 v[26:29], v176 offset:2048
	ds_read_b128 v[22:25], v177
	ds_read_b128 v[30:33], v177 offset:2048
	ds_read_b128 v[2:5], v178
	ds_read_b128 v[10:13], v178 offset:2048
	ds_read_b128 v[6:9], v179
	ds_read_b128 v[14:17], v179 offset:2048
	ds_read_b128 v[194:197], v180
	ds_read_b128 v[202:205], v180 offset:2048
	ds_read_b128 v[198:201], v181
	ds_read_b128 v[206:209], v181 offset:2048
	ds_read_b128 v[210:213], v180 offset:4096
	ds_read_b128 v[218:221], v180 offset:6144
	ds_read_b128 v[214:217], v181 offset:4096
	ds_read_b128 v[222:225], v181 offset:6144
	s_add_u32 s64, s12, s4
	s_addc_u32 s65, s13, s5
	s_add_u32 s46, s64, 0x80
	s_addc_u32 s47, s65, 0
	s_mov_b32 m0, s58
	s_nop 0
	global_load_lds_dwordx4 v163, s[46:47] offset:0
	s_nop 0
	s_mov_b32 m0, s59
	s_nop 0
	global_load_lds_dwordx4 v171, s[46:47] offset:0
	s_waitcnt vmcnt(8)
	s_waitcnt lgkmcnt(0)
	s_barrier
	s_setprio 1
	s_waitcnt lgkmcnt(0)
	v_mfma_f32_16x16x128_f8f6f4 v[158:161], v[18:25], v[194:201], 0
	v_mfma_f32_16x16x128_f8f6f4 v[154:157], v[26:33], v[194:201], 0
	v_mfma_f32_16x16x128_f8f6f4 v[142:145], v[18:25], v[202:209], 0
	v_mfma_f32_16x16x128_f8f6f4 v[138:141], v[26:33], v[202:209], 0
	v_mfma_f32_16x16x128_f8f6f4 v[126:129], v[18:25], v[210:217], 0
	v_mfma_f32_16x16x128_f8f6f4 v[122:125], v[26:33], v[210:217], 0
	v_mfma_f32_16x16x128_f8f6f4 v[110:113], v[18:25], v[218:225], 0
	v_mfma_f32_16x16x128_f8f6f4 v[106:109], v[26:33], v[218:225], 0
	s_setprio 0
	s_setprio 1
	v_mfma_f32_16x16x128_f8f6f4 v[150:153], v[2:9], v[194:201], 0
	v_mfma_f32_16x16x128_f8f6f4 v[146:149], v[10:17], v[194:201], 0
	v_mfma_f32_16x16x128_f8f6f4 v[134:137], v[2:9], v[202:209], 0
	v_mfma_f32_16x16x128_f8f6f4 v[130:133], v[10:17], v[202:209], 0
	v_mfma_f32_16x16x128_f8f6f4 v[118:121], v[2:9], v[210:217], 0
	v_mfma_f32_16x16x128_f8f6f4 v[114:117], v[10:17], v[210:217], 0
	v_mfma_f32_16x16x128_f8f6f4 v[102:105], v[2:9], v[218:225], 0
	v_mfma_f32_16x16x128_f8f6f4 v[98:101], v[10:17], v[218:225], 0
	s_setprio 0
	s_barrier
	s_add_u32 s66, s42, s4
	s_addc_u32 s67, s43, s5
	ds_read_b128 v[194:197], v180 offset:16384
	ds_read_b128 v[202:205], v180 offset:18432
	ds_read_b128 v[198:201], v181 offset:16384
	ds_read_b128 v[206:209], v181 offset:18432
	ds_read_b128 v[210:213], v180 offset:20480
	ds_read_b128 v[218:221], v180 offset:22528
	ds_read_b128 v[214:217], v181 offset:20480
	ds_read_b128 v[222:225], v181 offset:22528
	s_add_u32 s46, s66, 0x100
	s_addc_u32 s47, s67, 0
	s_mov_b32 m0, s33
	s_nop 0
	global_load_lds_dwordx4 v172, s[46:47] offset:0
	s_nop 0
	s_mov_b32 m0, s39
	s_nop 0
	global_load_lds_dwordx4 v173, s[46:47] offset:0
	s_add_u32 s46, s66, 0x20100
	s_addc_u32 s47, s67, 0
	s_mov_b32 m0, s41
	s_nop 0
	global_load_lds_dwordx4 v172, s[46:47] offset:0
	s_nop 0
	s_mov_b32 m0, s48
	s_nop 0
	global_load_lds_dwordx4 v173, s[46:47] offset:0
	s_add_u32 s46, s64, 0x100
	s_addc_u32 s47, s65, 0
	s_mov_b32 m0, s1
	s_nop 0
	global_load_lds_dwordx4 v162, s[46:47] offset:0
	s_nop 0
	s_mov_b32 m0, s49
	s_nop 0
	global_load_lds_dwordx4 v170, s[46:47] offset:0
	s_waitcnt vmcnt(8)
	s_waitcnt lgkmcnt(0)
	s_barrier
	s_setprio 1
	s_waitcnt lgkmcnt(5)
	v_mfma_f32_16x16x128_f8f6f4 v[94:97], v[18:25], v[194:201], 0
	v_mfma_f32_16x16x128_f8f6f4 v[90:93], v[26:33], v[194:201], 0
	s_waitcnt lgkmcnt(4)
	v_mfma_f32_16x16x128_f8f6f4 v[78:81], v[18:25], v[202:209], 0
	v_mfma_f32_16x16x128_f8f6f4 v[74:77], v[26:33], v[202:209], 0
	s_waitcnt lgkmcnt(1)
	v_mfma_f32_16x16x128_f8f6f4 v[62:65], v[18:25], v[210:217], 0
	v_mfma_f32_16x16x128_f8f6f4 v[58:61], v[26:33], v[210:217], 0
	s_waitcnt lgkmcnt(0)
	v_mfma_f32_16x16x128_f8f6f4 v[46:49], v[18:25], v[218:225], 0
	v_mfma_f32_16x16x128_f8f6f4 v[42:45], v[26:33], v[218:225], 0
	s_setprio 0
	s_setprio 1
	v_mfma_f32_16x16x128_f8f6f4 v[86:89], v[2:9], v[194:201], 0
	v_mfma_f32_16x16x128_f8f6f4 v[82:85], v[10:17], v[194:201], 0
	v_mfma_f32_16x16x128_f8f6f4 v[70:73], v[2:9], v[202:209], 0
	v_mfma_f32_16x16x128_f8f6f4 v[66:69], v[10:17], v[202:209], 0
	v_mfma_f32_16x16x128_f8f6f4 v[54:57], v[2:9], v[210:217], 0
	v_mfma_f32_16x16x128_f8f6f4 v[50:53], v[10:17], v[210:217], 0
	v_mfma_f32_16x16x128_f8f6f4 v[38:41], v[2:9], v[218:225], 0
	v_mfma_f32_16x16x128_f8f6f4 v[34:37], v[10:17], v[218:225], 0
	s_setprio 0
	s_barrier
	s_add_i32 s68, 0, 0x18000
	v_add_u32_e32 v183, s68, v174
	v_add_u32_e32 v184, s68, v175
	s_add_i32 s68, 0, 0x1c000
	v_add_u32_e32 v185, s68, v174
	ds_read_b128 v[2:5], v183
	ds_read_b128 v[10:13], v183 offset:2048
	ds_read_b128 v[6:9], v184
	ds_read_b128 v[14:17], v184 offset:2048
	v_add_u32_e32 v186, s68, v175
	ds_read_b128 v[18:21], v185
	ds_read_b128 v[26:29], v185 offset:2048
	ds_read_b128 v[22:25], v186
	ds_read_b128 v[30:33], v186 offset:2048
	ds_read_b128 v[194:197], v180 offset:32768
	ds_read_b128 v[202:205], v180 offset:34816
	ds_read_b128 v[198:201], v181 offset:32768
	ds_read_b128 v[206:209], v181 offset:34816
	ds_read_b128 v[210:213], v180 offset:36864
	ds_read_b128 v[218:221], v180 offset:38912
	ds_read_b128 v[214:217], v181 offset:36864
	ds_read_b128 v[222:225], v181 offset:38912
	s_mov_b32 m0, s50
	s_nop 0
	global_load_lds_dwordx4 v163, s[46:47] offset:0
	s_nop 0
	s_mov_b32 m0, s51
	s_nop 0
	global_load_lds_dwordx4 v171, s[46:47] offset:0
	s_waitcnt vmcnt(8)
	s_waitcnt lgkmcnt(0)
	s_barrier
	s_setprio 1
	s_waitcnt lgkmcnt(5)
	v_mfma_f32_16x16x128_f8f6f4 v[158:161], v[2:9], v[194:201], v[158:161]
	v_mfma_f32_16x16x128_f8f6f4 v[154:157], v[10:17], v[194:201], v[154:157]
	s_waitcnt lgkmcnt(4)
	v_mfma_f32_16x16x128_f8f6f4 v[142:145], v[2:9], v[202:209], v[142:145]
	v_mfma_f32_16x16x128_f8f6f4 v[138:141], v[10:17], v[202:209], v[138:141]
	s_waitcnt lgkmcnt(1)
	v_mfma_f32_16x16x128_f8f6f4 v[126:129], v[2:9], v[210:217], v[126:129]
	v_mfma_f32_16x16x128_f8f6f4 v[122:125], v[10:17], v[210:217], v[122:125]
	s_waitcnt lgkmcnt(0)
	v_mfma_f32_16x16x128_f8f6f4 v[110:113], v[2:9], v[218:225], v[110:113]
	v_mfma_f32_16x16x128_f8f6f4 v[106:109], v[10:17], v[218:225], v[106:109]
	s_setprio 0
	s_setprio 1
	v_mfma_f32_16x16x128_f8f6f4 v[150:153], v[18:25], v[194:201], v[150:153]
	v_mfma_f32_16x16x128_f8f6f4 v[146:149], v[26:33], v[194:201], v[146:149]
	v_mfma_f32_16x16x128_f8f6f4 v[134:137], v[18:25], v[202:209], v[134:137]
	v_mfma_f32_16x16x128_f8f6f4 v[130:133], v[26:33], v[202:209], v[130:133]
	v_mfma_f32_16x16x128_f8f6f4 v[118:121], v[18:25], v[210:217], v[118:121]
	v_mfma_f32_16x16x128_f8f6f4 v[114:117], v[26:33], v[210:217], v[114:117]
	v_mfma_f32_16x16x128_f8f6f4 v[102:105], v[18:25], v[218:225], v[102:105]
	v_mfma_f32_16x16x128_f8f6f4 v[98:101], v[26:33], v[218:225], v[98:101]
	s_setprio 0
	s_barrier
	ds_read_b128 v[194:197], v180 offset:49152
	ds_read_b128 v[202:205], v180 offset:51200
	ds_read_b128 v[198:201], v181 offset:49152
	ds_read_b128 v[206:209], v181 offset:51200
	ds_read_b128 v[210:213], v180 offset:53248
	ds_read_b128 v[218:221], v180 offset:55296
	ds_read_b128 v[214:217], v181 offset:53248
	ds_read_b128 v[222:225], v181 offset:55296
	s_add_u32 s46, s66, 0x180
	s_addc_u32 s47, s67, 0
	s_mov_b32 m0, s52
	s_nop 0
	global_load_lds_dwordx4 v172, s[46:47] offset:0
	s_nop 0
	s_mov_b32 m0, s53
	s_nop 0
	global_load_lds_dwordx4 v173, s[46:47] offset:0
	s_add_u32 s46, s66, 0x20180
	s_addc_u32 s47, s67, 0
	s_mov_b32 m0, s56
	s_nop 0
	global_load_lds_dwordx4 v172, s[46:47] offset:0
	s_nop 0
	s_mov_b32 m0, s57
	s_nop 0
	global_load_lds_dwordx4 v173, s[46:47] offset:0
	s_add_u32 s46, s64, 0x180
	s_addc_u32 s47, s65, 0
	s_mov_b32 m0, s54
	s_nop 0
	global_load_lds_dwordx4 v162, s[46:47] offset:0
	s_nop 0
	s_mov_b32 m0, s55
	s_nop 0
	global_load_lds_dwordx4 v170, s[46:47] offset:0
	s_waitcnt vmcnt(8)
	s_waitcnt lgkmcnt(0)
	s_barrier
	s_setprio 1
	s_waitcnt lgkmcnt(5)
	v_mfma_f32_16x16x128_f8f6f4 v[94:97], v[2:9], v[194:201], v[94:97]
	v_mfma_f32_16x16x128_f8f6f4 v[90:93], v[10:17], v[194:201], v[90:93]
	s_waitcnt lgkmcnt(4)
	v_mfma_f32_16x16x128_f8f6f4 v[78:81], v[2:9], v[202:209], v[78:81]
	v_mfma_f32_16x16x128_f8f6f4 v[74:77], v[10:17], v[202:209], v[74:77]
	s_waitcnt lgkmcnt(1)
	v_mfma_f32_16x16x128_f8f6f4 v[62:65], v[2:9], v[210:217], v[62:65]
	v_mfma_f32_16x16x128_f8f6f4 v[58:61], v[10:17], v[210:217], v[58:61]
	s_waitcnt lgkmcnt(0)
	v_mfma_f32_16x16x128_f8f6f4 v[46:49], v[2:9], v[218:225], v[46:49]
	v_mfma_f32_16x16x128_f8f6f4 v[42:45], v[10:17], v[218:225], v[42:45]
	s_setprio 0
	s_setprio 1
	v_mfma_f32_16x16x128_f8f6f4 v[86:89], v[18:25], v[194:201], v[86:89]
	v_mfma_f32_16x16x128_f8f6f4 v[82:85], v[26:33], v[194:201], v[82:85]
	v_mfma_f32_16x16x128_f8f6f4 v[70:73], v[18:25], v[202:209], v[70:73]
	v_mfma_f32_16x16x128_f8f6f4 v[66:69], v[26:33], v[202:209], v[66:69]
	v_mfma_f32_16x16x128_f8f6f4 v[54:57], v[18:25], v[210:217], v[54:57]
	v_mfma_f32_16x16x128_f8f6f4 v[50:53], v[26:33], v[210:217], v[50:53]
	v_mfma_f32_16x16x128_f8f6f4 v[38:41], v[18:25], v[218:225], v[38:41]
	v_mfma_f32_16x16x128_f8f6f4 v[34:37], v[26:33], v[218:225], v[34:37]
	s_setprio 0
	s_add_i32 s35, s35, 2
	s_add_u32 s4, s4, 0x100
	s_addc_u32 s5, s5, 0
	s_barrier
	.p2align 6
